# 72 converter workgroups + s_setprio flipped in both expert GEMM phases (loader segments prio 1)
# speedup vs baseline: 1.0183x; 1.0125x over previous
; #define LAS __attribute__((address_space(3)))
; #define PG8_STAGEB(bufoff, gbase) PG8_STAGE2(bufoff, gbase, voffB[0], voffB[1])
; #define PG8_STAGEA(bufoff, gbase, h) PG8_STAGE2(bufoff, gbase, voffA[h][0], voffA[h][1])
; #define PG8_STAGEAS(bufoff, gbase, h) PG8_STAGE2(bufoff, gbase, voffA[h][0], voffA[h][1])
; #define PG8_LDA(dst, b, h) do { _Pragma("unroll") for (int m = 0; m < 4; ++m) _Pragma("unroll") for (int k = 0; k < 2; ++k) dst[m][k] = *(const LAS bf16x8*)(lds + PG8_SA(b, h) + aoff + m * 2048 + k * 1024); } while (0)
; #define PG8_LDB(dst, b, h) do { _Pragma("unroll") for (int n = 0; n < 2; ++n) _Pragma("unroll") for (int k = 0; k < 2; ++k) dst[n][k] = *(const LAS bf16x8*)(lds + PG8_SB(b, h) + boff + n * 2048 + k * 1024); } while (0)
; #define PG8_WAIT_K0() do { if (EST > 0 && t == 0 && ui > 0) asm volatile("s_waitcnt vmcnt(%0)" :: "n"((HM ? 6 : 8) + EST) : "memory"); else PG8_WAIT_K(); } while (0)
; #define PG8_WAIT_L(n) asm volatile("s_waitcnt lgkmcnt(" #n ")" ::: "memory")
; #define PG8_BAR __builtin_amdgcn_s_barrier()
; #define PG8_SCHED __builtin_amdgcn_sched_barrier(0)
;     ...
;             const char* a1 = cA + (size_t)(t + 1) * kstep;
;             const char* a2 = last ? nA : cA + (size_t)(t + 2) * kstep; const char* b2 = last ? nB : cB + (size_t)(t + 2) * kstep;
;             const char* a3 = a2 + kstep; const char* b3 = b2 + kstep;
;             PG8_LDB(B0, 0, 0); PG8_LDB(B1, 0, 1); PG8_SCHED; PG8_LDA(At, 0, 0); if constexpr (!HM) PG8_STAGEA(PG8_SA(1, 1), a1, 1);
;             if constexpr (Sched::kGather) { if (last && has_next) { const u32x4 tn = *(const LAS u32x4*)(S.aux + tid * 16); voffA[0][0] = tn.x; voffA[0][1] = tn.y; voffA[1][0] = tn.z; voffA[1][1] = tn.w; } }
;             PG8_WAIT_K0(); PG8_WAIT_L(0); PG8_BAR; PG8_MMA(0, 0, At, B0); PG8_MMA(0, 1, At, B1); PG8_BAR; PG8_SCHED;
;             if constexpr (!HM) PG8_LDA(At, 0, 1);
;             PG8_STAGEB(PG8_SB(0, 0), b2); PG8_STAGEB(PG8_SB(0, 1), b2 + hstepB); PG8_STAGEAS(PG8_SA(0, 0), a2, 0);
;             PG8_WAIT_K0(); PG8_WAIT_L(0); PG8_BAR; if constexpr (!HM) { PG8_MMA(1, 0, At, B0); PG8_MMA(1, 1, At, B1); } PG8_BAR; PG8_SCHED;
.LBB0_1290:
	ds_read_b128 v[26:29], v184
	ds_read_b128 v[30:33], v184 offset:1024
	ds_read_b128 v[18:21], v184 offset:2048
	ds_read_b128 v[22:25], v184 offset:3072
	ds_read_b128 v[10:13], v185
	ds_read_b128 v[14:17], v185 offset:1024
	ds_read_b128 v[2:5], v185 offset:2048
	ds_read_b128 v[6:9], v185 offset:3072
	s_cmp_eq_u32 s73, 12
	s_cselect_b32 s42, s0, s25
	s_cselect_b32 s43, s1, s27
	s_cselect_b32 s40, s30, s29
	s_cselect_b32 s41, s31, s72
	s_add_u32 s38, s42, 0x80
	s_addc_u32 s39, s43, 0
	ds_read_b128 v[190:193], v186
	ds_read_b128 v[194:197], v186 offset:1024
	ds_read_b128 v[198:201], v186 offset:2048
	ds_read_b128 v[202:205], v186 offset:3072
	ds_read_b128 v[206:209], v186 offset:4096
	ds_read_b128 v[210:213], v186 offset:5120
	ds_read_b128 v[214:217], v186 offset:6144
	ds_read_b128 v[218:221], v186 offset:7168
	s_mov_b32 s74, m0
	s_mov_b32 m0, s68
	s_nop 0
	global_load_lds_dwordx4 v167, s[36:37]
	s_mov_b32 m0, s74
	s_nop 0
	s_mov_b32 s74, m0
	s_mov_b32 m0, s69
	s_nop 0
	global_load_lds_dwordx4 v168, s[36:37]
	s_mov_b32 m0, s74
	s_waitcnt vmcnt(8)
	s_waitcnt lgkmcnt(0)
	s_barrier
	s_setprio 0
	s_waitcnt lgkmcnt(6)
	v_mfma_scale_f32_16x16x128_f8f6f4 v[158:161], v[26:33], v[190:197], v[158:161], v1, v164 op_sel_hi:[0,0,0]
	v_mfma_scale_f32_16x16x128_f8f6f4 v[154:157], v[18:25], v[190:197], v[154:157], v1, v164 op_sel_hi:[0,0,0]
	s_waitcnt lgkmcnt(4)
	v_mfma_scale_f32_16x16x128_f8f6f4 v[142:145], v[26:33], v[198:205], v[142:145], v1, v164 op_sel_hi:[0,0,0]
	v_mfma_scale_f32_16x16x128_f8f6f4 v[138:141], v[18:25], v[198:205], v[138:141], v1, v164 op_sel_hi:[0,0,0]
	s_waitcnt lgkmcnt(2)
	v_mfma_scale_f32_16x16x128_f8f6f4 v[126:129], v[26:33], v[206:213], v[126:129], v1, v164 op_sel_hi:[0,0,0]
	v_mfma_scale_f32_16x16x128_f8f6f4 v[122:125], v[18:25], v[206:213], v[122:125], v1, v164 op_sel_hi:[0,0,0]
	s_waitcnt lgkmcnt(0)
	v_mfma_scale_f32_16x16x128_f8f6f4 v[110:113], v[26:33], v[214:221], v[110:113], v1, v164 op_sel_hi:[0,0,0]
	v_mfma_scale_f32_16x16x128_f8f6f4 v[106:109], v[18:25], v[214:221], v[106:109], v1, v164 op_sel_hi:[0,0,0]
	s_setprio 1
	s_setprio 0
	v_mfma_scale_f32_16x16x128_f8f6f4 v[150:153], v[10:17], v[190:197], v[150:153], v1, v164 op_sel_hi:[0,0,0]
	v_mfma_scale_f32_16x16x128_f8f6f4 v[146:149], v[2:9], v[190:197], v[146:149], v1, v164 op_sel_hi:[0,0,0]
	v_mfma_scale_f32_16x16x128_f8f6f4 v[134:137], v[10:17], v[198:205], v[134:137], v1, v164 op_sel_hi:[0,0,0]
	v_mfma_scale_f32_16x16x128_f8f6f4 v[130:133], v[2:9], v[198:205], v[130:133], v1, v164 op_sel_hi:[0,0,0]
	v_mfma_scale_f32_16x16x128_f8f6f4 v[118:121], v[10:17], v[206:213], v[118:121], v1, v164 op_sel_hi:[0,0,0]
	v_mfma_scale_f32_16x16x128_f8f6f4 v[114:117], v[2:9], v[206:213], v[114:117], v1, v164 op_sel_hi:[0,0,0]
	v_mfma_scale_f32_16x16x128_f8f6f4 v[102:105], v[10:17], v[214:221], v[102:105], v1, v164 op_sel_hi:[0,0,0]
	v_mfma_scale_f32_16x16x128_f8f6f4 v[98:101], v[2:9], v[214:221], v[98:101], v1, v164 op_sel_hi:[0,0,0]
	s_setprio 1
	s_barrier
	ds_read_b128 v[190:193], v186 offset:16384
	ds_read_b128 v[194:197], v186 offset:17408
	ds_read_b128 v[198:201], v186 offset:18432
	ds_read_b128 v[202:205], v186 offset:19456
	ds_read_b128 v[206:209], v186 offset:20480
	ds_read_b128 v[210:213], v186 offset:21504
	ds_read_b128 v[214:217], v186 offset:22528
	ds_read_b128 v[218:221], v186 offset:23552
	s_mov_b32 s74, m0
	s_mov_b32 m0, s55
	s_nop 0
	global_load_lds_dwordx4 v169, s[40:41]
	s_mov_b32 m0, s74
	s_nop 0
	s_mov_b32 s74, m0
	s_mov_b32 m0, s56
	s_nop 0
	global_load_lds_dwordx4 v170, s[40:41]
	s_mov_b32 m0, s74
	s_add_u32 s74, s40, 0x40000
	s_addc_u32 s75, s41, 0
	s_mov_b32 s76, m0
	s_mov_b32 m0, s57
	s_nop 0
	global_load_lds_dwordx4 v169, s[74:75]
	s_mov_b32 m0, s76
	s_nop 0
	s_mov_b32 s76, m0
	s_mov_b32 m0, s58
	s_nop 0
	global_load_lds_dwordx4 v170, s[74:75]
	s_mov_b32 m0, s76
	s_mov_b32 s74, m0
	s_mov_b32 m0, s54
	s_nop 0
	global_load_lds_dwordx4 v165, s[42:43]
	s_mov_b32 m0, s74
	s_nop 0
	s_mov_b32 s74, m0
	s_mov_b32 m0, s59
	s_nop 0
	global_load_lds_dwordx4 v166, s[42:43]
	s_mov_b32 m0, s74
	s_waitcnt vmcnt(8)
	s_waitcnt lgkmcnt(0)
	s_barrier
	s_setprio 0
	s_waitcnt lgkmcnt(6)
	v_mfma_scale_f32_16x16x128_f8f6f4 v[94:97], v[26:33], v[190:197], v[94:97], v1, v164 op_sel_hi:[0,0,0]
	v_mfma_scale_f32_16x16x128_f8f6f4 v[90:93], v[18:25], v[190:197], v[90:93], v1, v164 op_sel_hi:[0,0,0]
	s_waitcnt lgkmcnt(4)
	v_mfma_scale_f32_16x16x128_f8f6f4 v[78:81], v[26:33], v[198:205], v[78:81], v1, v164 op_sel_hi:[0,0,0]
	v_mfma_scale_f32_16x16x128_f8f6f4 v[74:77], v[18:25], v[198:205], v[74:77], v1, v164 op_sel_hi:[0,0,0]
	s_waitcnt lgkmcnt(2)
	v_mfma_scale_f32_16x16x128_f8f6f4 v[62:65], v[26:33], v[206:213], v[62:65], v1, v164 op_sel_hi:[0,0,0]
	v_mfma_scale_f32_16x16x128_f8f6f4 v[58:61], v[18:25], v[206:213], v[58:61], v1, v164 op_sel_hi:[0,0,0]
	s_waitcnt lgkmcnt(0)
	v_mfma_scale_f32_16x16x128_f8f6f4 v[46:49], v[26:33], v[214:221], v[46:49], v1, v164 op_sel_hi:[0,0,0]
	v_mfma_scale_f32_16x16x128_f8f6f4 v[42:45], v[18:25], v[214:221], v[42:45], v1, v164 op_sel_hi:[0,0,0]
	s_setprio 1
	s_setprio 0
	v_mfma_scale_f32_16x16x128_f8f6f4 v[86:89], v[10:17], v[190:197], v[86:89], v1, v164 op_sel_hi:[0,0,0]
	v_mfma_scale_f32_16x16x128_f8f6f4 v[82:85], v[2:9], v[190:197], v[82:85], v1, v164 op_sel_hi:[0,0,0]
	v_mfma_scale_f32_16x16x128_f8f6f4 v[70:73], v[10:17], v[198:205], v[70:73], v1, v164 op_sel_hi:[0,0,0]
	v_mfma_scale_f32_16x16x128_f8f6f4 v[66:69], v[2:9], v[198:205], v[66:69], v1, v164 op_sel_hi:[0,0,0]
	v_mfma_scale_f32_16x16x128_f8f6f4 v[54:57], v[10:17], v[206:213], v[54:57], v1, v164 op_sel_hi:[0,0,0]
	v_mfma_scale_f32_16x16x128_f8f6f4 v[50:53], v[2:9], v[206:213], v[50:53], v1, v164 op_sel_hi:[0,0,0]
	v_mfma_scale_f32_16x16x128_f8f6f4 v[38:41], v[10:17], v[214:221], v[38:41], v1, v164 op_sel_hi:[0,0,0]
	v_mfma_scale_f32_16x16x128_f8f6f4 v[34:37], v[2:9], v[214:221], v[34:37], v1, v164 op_sel_hi:[0,0,0]
	s_setprio 1
	s_barrier
; #define PG8_STAGEB(bufoff, gbase) PG8_STAGE2(bufoff, gbase, voffB[0], voffB[1])
; #define PG8_STAGEAS(bufoff, gbase, h) PG8_STAGE2(bufoff, gbase, voffA[h][0], voffA[h][1])
; #define PG8_LDA(dst, b, h) do { _Pragma("unroll") for (int m = 0; m < 4; ++m) _Pragma("unroll") for (int k = 0; k < 2; ++k) dst[m][k] = *(const LAS bf16x8*)(lds + PG8_SA(b, h) + aoff + m * 2048 + k * 1024); } while (0)
; #define PG8_LDB(dst, b, h) do { _Pragma("unroll") for (int n = 0; n < 2; ++n) _Pragma("unroll") for (int k = 0; k < 2; ++k) dst[n][k] = *(const LAS bf16x8*)(lds + PG8_SB(b, h) + boff + n * 2048 + k * 1024); } while (0)
; #define PG8_WAIT_K() do { if constexpr (HM) PG8_WAIT_V(6); else PG8_WAIT_V(8); } while (0)
; #define PG8_WAIT_L(n) asm volatile("s_waitcnt lgkmcnt(" #n ")" ::: "memory")
; #define PG8_BAR __builtin_amdgcn_s_barrier()
; #define PG8_SCHED __builtin_amdgcn_sched_barrier(0)
;     ...
;             PG8_LDB(B0, 1, 0); PG8_LDB(B1, 1, 1); PG8_SCHED; PG8_LDA(At, 1, 0); if constexpr (!HM) PG8_STAGEAS(PG8_SA(0, 1), a2, 1);
;             PG8_WAIT_K(); PG8_WAIT_L(0); PG8_BAR; PG8_MMA(0, 0, At, B0); PG8_MMA(0, 1, At, B1); PG8_BAR; PG8_SCHED;
;             if constexpr (!HM) PG8_LDA(At, 1, 1);
;             PG8_STAGEB(PG8_SB(1, 0), b3); PG8_STAGEB(PG8_SB(1, 1), b3 + hstepB); PG8_STAGEAS(PG8_SA(1, 0), a3, 0);
;             PG8_WAIT_K(); PG8_WAIT_L(0); PG8_BAR; if constexpr (!HM) { PG8_MMA(1, 0, At, B0); PG8_MMA(1, 1, At, B1); } PG8_BAR; PG8_SCHED;
;         }
	ds_read_b128 v[2:5], v187
	ds_read_b128 v[6:9], v187 offset:1024
	ds_read_b128 v[10:13], v187 offset:2048
	ds_read_b128 v[14:17], v187 offset:3072
	ds_read_b128 v[18:21], v188
	ds_read_b128 v[22:25], v188 offset:1024
	ds_read_b128 v[26:29], v188 offset:2048
	ds_read_b128 v[30:33], v188 offset:3072
	ds_read_b128 v[190:193], v186 offset:32768
	ds_read_b128 v[194:197], v186 offset:33792
	ds_read_b128 v[198:201], v186 offset:34816
	ds_read_b128 v[202:205], v186 offset:35840
	ds_read_b128 v[206:209], v186 offset:36864
	ds_read_b128 v[210:213], v186 offset:37888
	ds_read_b128 v[214:217], v186 offset:38912
	ds_read_b128 v[218:221], v186 offset:39936
	s_mov_b32 s74, m0
	s_mov_b32 m0, s60
	s_nop 0
	global_load_lds_dwordx4 v167, s[42:43]
	s_mov_b32 m0, s74
	s_nop 0
	s_mov_b32 s74, m0
	s_mov_b32 m0, s61
	s_nop 0
	global_load_lds_dwordx4 v168, s[42:43]
	s_mov_b32 m0, s74
	s_waitcnt vmcnt(8)
	s_waitcnt lgkmcnt(0)
	s_barrier
	s_setprio 0
	s_waitcnt lgkmcnt(6)
	v_mfma_scale_f32_16x16x128_f8f6f4 v[158:161], v[2:9], v[190:197], v[158:161], v1, v164 op_sel_hi:[0,0,0]
	v_mfma_scale_f32_16x16x128_f8f6f4 v[154:157], v[10:17], v[190:197], v[154:157], v1, v164 op_sel_hi:[0,0,0]
	s_waitcnt lgkmcnt(4)
	v_mfma_scale_f32_16x16x128_f8f6f4 v[142:145], v[2:9], v[198:205], v[142:145], v1, v164 op_sel_hi:[0,0,0]
	v_mfma_scale_f32_16x16x128_f8f6f4 v[138:141], v[10:17], v[198:205], v[138:141], v1, v164 op_sel_hi:[0,0,0]
	s_waitcnt lgkmcnt(2)
	v_mfma_scale_f32_16x16x128_f8f6f4 v[126:129], v[2:9], v[206:213], v[126:129], v1, v164 op_sel_hi:[0,0,0]
	v_mfma_scale_f32_16x16x128_f8f6f4 v[122:125], v[10:17], v[206:213], v[122:125], v1, v164 op_sel_hi:[0,0,0]
	s_waitcnt lgkmcnt(0)
	v_mfma_scale_f32_16x16x128_f8f6f4 v[110:113], v[2:9], v[214:221], v[110:113], v1, v164 op_sel_hi:[0,0,0]
	v_mfma_scale_f32_16x16x128_f8f6f4 v[106:109], v[10:17], v[214:221], v[106:109], v1, v164 op_sel_hi:[0,0,0]
	s_setprio 1
	s_setprio 0
	v_mfma_scale_f32_16x16x128_f8f6f4 v[150:153], v[18:25], v[190:197], v[150:153], v1, v164 op_sel_hi:[0,0,0]
	v_mfma_scale_f32_16x16x128_f8f6f4 v[146:149], v[26:33], v[190:197], v[146:149], v1, v164 op_sel_hi:[0,0,0]
	v_mfma_scale_f32_16x16x128_f8f6f4 v[134:137], v[18:25], v[198:205], v[134:137], v1, v164 op_sel_hi:[0,0,0]
	v_mfma_scale_f32_16x16x128_f8f6f4 v[130:133], v[26:33], v[198:205], v[130:133], v1, v164 op_sel_hi:[0,0,0]
	v_mfma_scale_f32_16x16x128_f8f6f4 v[118:121], v[18:25], v[206:213], v[118:121], v1, v164 op_sel_hi:[0,0,0]
	v_mfma_scale_f32_16x16x128_f8f6f4 v[114:117], v[26:33], v[206:213], v[114:117], v1, v164 op_sel_hi:[0,0,0]
	v_mfma_scale_f32_16x16x128_f8f6f4 v[102:105], v[18:25], v[214:221], v[102:105], v1, v164 op_sel_hi:[0,0,0]
	v_mfma_scale_f32_16x16x128_f8f6f4 v[98:101], v[26:33], v[214:221], v[98:101], v1, v164 op_sel_hi:[0,0,0]
	s_setprio 1
	s_barrier
	ds_read_b128 v[190:193], v186 offset:49152
	ds_read_b128 v[194:197], v186 offset:50176
	ds_read_b128 v[198:201], v186 offset:51200
	ds_read_b128 v[202:205], v186 offset:52224
	ds_read_b128 v[206:209], v186 offset:53248
	ds_read_b128 v[210:213], v186 offset:54272
	ds_read_b128 v[214:217], v186 offset:55296
	ds_read_b128 v[218:221], v186 offset:56320
	s_add_u32 s42, s40, 0x80
	s_addc_u32 s43, s41, 0
	s_mov_b32 s74, m0
	s_mov_b32 m0, s62
	s_nop 0
	global_load_lds_dwordx4 v169, s[42:43]
	s_mov_b32 m0, s74
	s_add_u32 s40, s40, 0x40080
	s_mov_b32 s74, m0
	s_mov_b32 m0, s63
	s_nop 0
	global_load_lds_dwordx4 v170, s[42:43]
	s_mov_b32 m0, s74
	s_addc_u32 s41, s41, 0
	s_mov_b32 s42, m0
	s_mov_b32 m0, s66
	s_nop 0
	global_load_lds_dwordx4 v169, s[40:41]
	s_mov_b32 m0, s42
	s_nop 0
	s_mov_b32 s42, m0
	s_mov_b32 m0, s67
	s_nop 0
	global_load_lds_dwordx4 v170, s[40:41]
	s_mov_b32 m0, s42
	s_mov_b32 s40, m0
	s_mov_b32 m0, s64
	s_nop 0
	global_load_lds_dwordx4 v165, s[38:39]
	s_mov_b32 m0, s40
	s_nop 0
	s_mov_b32 s40, m0
	s_mov_b32 m0, s65
	s_nop 0
	global_load_lds_dwordx4 v166, s[38:39]
	s_mov_b32 m0, s40
	s_waitcnt vmcnt(8)
	s_waitcnt lgkmcnt(0)
	s_barrier
	s_setprio 0
	s_waitcnt lgkmcnt(6)
	v_mfma_scale_f32_16x16x128_f8f6f4 v[94:97], v[2:9], v[190:197], v[94:97], v1, v164 op_sel_hi:[0,0,0]
	v_mfma_scale_f32_16x16x128_f8f6f4 v[90:93], v[10:17], v[190:197], v[90:93], v1, v164 op_sel_hi:[0,0,0]
	s_waitcnt lgkmcnt(4)
	v_mfma_scale_f32_16x16x128_f8f6f4 v[78:81], v[2:9], v[198:205], v[78:81], v1, v164 op_sel_hi:[0,0,0]
	v_mfma_scale_f32_16x16x128_f8f6f4 v[74:77], v[10:17], v[198:205], v[74:77], v1, v164 op_sel_hi:[0,0,0]
	s_waitcnt lgkmcnt(2)
	v_mfma_scale_f32_16x16x128_f8f6f4 v[62:65], v[2:9], v[206:213], v[62:65], v1, v164 op_sel_hi:[0,0,0]
	v_mfma_scale_f32_16x16x128_f8f6f4 v[58:61], v[10:17], v[206:213], v[58:61], v1, v164 op_sel_hi:[0,0,0]
	s_waitcnt lgkmcnt(0)
	v_mfma_scale_f32_16x16x128_f8f6f4 v[46:49], v[2:9], v[214:221], v[46:49], v1, v164 op_sel_hi:[0,0,0]
	v_mfma_scale_f32_16x16x128_f8f6f4 v[42:45], v[10:17], v[214:221], v[42:45], v1, v164 op_sel_hi:[0,0,0]
	s_setprio 1
	s_setprio 0
	v_mfma_scale_f32_16x16x128_f8f6f4 v[86:89], v[18:25], v[190:197], v[86:89], v1, v164 op_sel_hi:[0,0,0]
	v_mfma_scale_f32_16x16x128_f8f6f4 v[82:85], v[26:33], v[190:197], v[82:85], v1, v164 op_sel_hi:[0,0,0]
	v_mfma_scale_f32_16x16x128_f8f6f4 v[70:73], v[18:25], v[198:205], v[70:73], v1, v164 op_sel_hi:[0,0,0]
	v_mfma_scale_f32_16x16x128_f8f6f4 v[66:69], v[26:33], v[198:205], v[66:69], v1, v164 op_sel_hi:[0,0,0]
	v_mfma_scale_f32_16x16x128_f8f6f4 v[54:57], v[18:25], v[206:213], v[54:57], v1, v164 op_sel_hi:[0,0,0]
	v_mfma_scale_f32_16x16x128_f8f6f4 v[50:53], v[26:33], v[206:213], v[50:53], v1, v164 op_sel_hi:[0,0,0]
	v_mfma_scale_f32_16x16x128_f8f6f4 v[38:41], v[18:25], v[214:221], v[38:41], v1, v164 op_sel_hi:[0,0,0]
	v_mfma_scale_f32_16x16x128_f8f6f4 v[34:37], v[26:33], v[214:221], v[34:37], v1, v164 op_sel_hi:[0,0,0]
	s_setprio 1
	s_barrier
	s_add_i32 s73, s73, 2
	s_add_u32 s25, s25, 0x100
	s_addc_u32 s27, s27, 0
	s_add_u32 s29, s29, 0x100
	s_addc_u32 s72, s72, 0
	s_add_u32 s36, s36, 0x100
	s_addc_u32 s37, s37, 0
	s_cmp_gt_u32 s73, 13
	s_cbranch_scc0 .LBB0_1290
	s_and_b64 vcc, exec, s[20:21]
	s_cbranch_vccz .LBB0_1293
	s_barrier

; #define LAS __attribute__((address_space(3)))
; #define PG8_STAGEB(bufoff, gbase) PG8_STAGE2(bufoff, gbase, voffB[0], voffB[1])
; #define PG8_STAGEA(bufoff, gbase, h) PG8_STAGE2(bufoff, gbase, voffA[h][0], voffA[h][1])
; #define PG8_STAGEAS(bufoff, gbase, h) PG8_STAGE2(bufoff, gbase, voffA[h][0], voffA[h][1])
; #define PG8_LDA(dst, b, h) do { _Pragma("unroll") for (int m = 0; m < 4; ++m) _Pragma("unroll") for (int k = 0; k < 2; ++k) dst[m][k] = *(const LAS bf16x8*)(lds + PG8_SA(b, h) + aoff + m * 2048 + k * 1024); } while (0)
; #define PG8_LDB(dst, b, h) do { _Pragma("unroll") for (int n = 0; n < 2; ++n) _Pragma("unroll") for (int k = 0; k < 2; ++k) dst[n][k] = *(const LAS bf16x8*)(lds + PG8_SB(b, h) + boff + n * 2048 + k * 1024); } while (0)
; #define PG8_WAIT_K0() do { if (EST > 0 && t == 0 && ui > 0) asm volatile("s_waitcnt vmcnt(%0)" :: "n"((HM ? 6 : 8) + EST) : "memory"); else PG8_WAIT_K(); } while (0)
; #define PG8_WAIT_L(n) asm volatile("s_waitcnt lgkmcnt(" #n ")" ::: "memory")
; #define PG8_BAR __builtin_amdgcn_s_barrier()
; #define PG8_SCHED __builtin_amdgcn_sched_barrier(0)
;     ...
;             PG8_LDB(B0, 0, 0); PG8_LDB(B1, 0, 1); PG8_SCHED; PG8_LDA(At, 0, 0); if constexpr (!HM) PG8_STAGEA(PG8_SA(1, 1), a1, 1);
;             if constexpr (Sched::kGather) { if (last && has_next) { const u32x4 tn = *(const LAS u32x4*)(S.aux + tid * 16); voffA[0][0] = tn.x; voffA[0][1] = tn.y; voffA[1][0] = tn.z; voffA[1][1] = tn.w; } }
;             PG8_WAIT_K0(); PG8_WAIT_L(0); PG8_BAR; PG8_MMA(0, 0, At, B0); PG8_MMA(0, 1, At, B1); PG8_BAR; PG8_SCHED;
;             if constexpr (!HM) PG8_LDA(At, 0, 1);
;             PG8_STAGEB(PG8_SB(0, 0), b2); PG8_STAGEB(PG8_SB(0, 1), b2 + hstepB); PG8_STAGEAS(PG8_SA(0, 0), a2, 0);
;             PG8_WAIT_K0(); PG8_WAIT_L(0); PG8_BAR; if constexpr (!HM) { PG8_MMA(1, 0, At, B0); PG8_MMA(1, 1, At, B1); } PG8_BAR; PG8_SCHED;
.LBB0_1346:
	ds_read_b128 v[68:71], v100
	ds_read_b128 v[72:75], v100 offset:1024
	ds_read_b128 v[76:79], v100 offset:2048
	ds_read_b128 v[80:83], v100 offset:3072
	ds_read_b128 v[106:109], v101
	ds_read_b128 v[110:113], v101 offset:1024
	ds_read_b128 v[114:117], v101 offset:2048
	ds_read_b128 v[118:121], v101 offset:3072
	s_cmp_eq_u32 s66, 12
	s_cselect_b32 s40, s0, s25
	s_cselect_b32 s41, s1, s29
	s_cselect_b32 s38, s34, s31
	s_cselect_b32 s39, s35, s65
	s_add_u32 s36, s40, 0x80
	s_addc_u32 s37, s41, 0
	ds_read_b128 v[122:125], v102
	ds_read_b128 v[126:129], v102 offset:1024
	ds_read_b128 v[130:133], v102 offset:2048
	ds_read_b128 v[134:137], v102 offset:3072
	ds_read_b128 v[138:141], v102 offset:4096
	ds_read_b128 v[142:145], v102 offset:5120
	ds_read_b128 v[146:149], v102 offset:6144
	ds_read_b128 v[150:153], v102 offset:7168
	s_waitcnt vmcnt(6)
	s_waitcnt lgkmcnt(0)
	s_barrier
	s_setprio 0
	s_waitcnt lgkmcnt(6)
	v_mfma_scale_f32_16x16x128_f8f6f4 v[62:65], v[68:75], v[122:129], v[62:65], v1, v86 op_sel_hi:[0,0,0]
	v_mfma_scale_f32_16x16x128_f8f6f4 v[58:61], v[76:83], v[122:129], v[58:61], v1, v86 op_sel_hi:[0,0,0]
	s_waitcnt lgkmcnt(4)
	v_mfma_scale_f32_16x16x128_f8f6f4 v[46:49], v[68:75], v[130:137], v[46:49], v1, v86 op_sel_hi:[0,0,0]
	v_mfma_scale_f32_16x16x128_f8f6f4 v[42:45], v[76:83], v[130:137], v[42:45], v1, v86 op_sel_hi:[0,0,0]
	s_waitcnt lgkmcnt(2)
	v_mfma_scale_f32_16x16x128_f8f6f4 v[30:33], v[68:75], v[138:145], v[30:33], v1, v86 op_sel_hi:[0,0,0]
	v_mfma_scale_f32_16x16x128_f8f6f4 v[26:29], v[76:83], v[138:145], v[26:29], v1, v86 op_sel_hi:[0,0,0]
	s_waitcnt lgkmcnt(0)
	v_mfma_scale_f32_16x16x128_f8f6f4 v[14:17], v[68:75], v[146:153], v[14:17], v1, v86 op_sel_hi:[0,0,0]
	v_mfma_scale_f32_16x16x128_f8f6f4 v[10:13], v[76:83], v[146:153], v[10:13], v1, v86 op_sel_hi:[0,0,0]
	s_setprio 1
	s_setprio 0
	v_mfma_scale_f32_16x16x128_f8f6f4 v[54:57], v[106:113], v[122:129], v[54:57], v1, v86 op_sel_hi:[0,0,0]
	v_mfma_scale_f32_16x16x128_f8f6f4 v[50:53], v[114:121], v[122:129], v[50:53], v1, v86 op_sel_hi:[0,0,0]
	v_mfma_scale_f32_16x16x128_f8f6f4 v[38:41], v[106:113], v[130:137], v[38:41], v1, v86 op_sel_hi:[0,0,0]
	v_mfma_scale_f32_16x16x128_f8f6f4 v[34:37], v[114:121], v[130:137], v[34:37], v1, v86 op_sel_hi:[0,0,0]
	v_mfma_scale_f32_16x16x128_f8f6f4 v[22:25], v[106:113], v[138:145], v[22:25], v1, v86 op_sel_hi:[0,0,0]
	v_mfma_scale_f32_16x16x128_f8f6f4 v[18:21], v[114:121], v[138:145], v[18:21], v1, v86 op_sel_hi:[0,0,0]
	v_mfma_scale_f32_16x16x128_f8f6f4 v[6:9], v[106:113], v[146:153], v[6:9], v1, v86 op_sel_hi:[0,0,0]
	v_mfma_scale_f32_16x16x128_f8f6f4 v[2:5], v[114:121], v[146:153], v[2:5], v1, v86 op_sel_hi:[0,0,0]
	s_setprio 1
	s_barrier
	s_mov_b32 s67, m0
	s_mov_b32 m0, s51
	s_nop 0
	global_load_lds_dwordx4 v89, s[38:39]
	s_mov_b32 m0, s67
	s_add_u32 s68, s38, 0x40000
	s_mov_b32 s67, m0
	s_mov_b32 m0, s52
	s_nop 0
	global_load_lds_dwordx4 v90, s[38:39]
	s_mov_b32 m0, s67
	s_addc_u32 s69, s39, 0
	s_mov_b32 s67, m0
	s_mov_b32 m0, s53
	s_nop 0
	global_load_lds_dwordx4 v89, s[68:69]
	s_mov_b32 m0, s67
	s_nop 0
	s_mov_b32 s67, m0
	s_mov_b32 m0, s54
	s_nop 0
	global_load_lds_dwordx4 v90, s[68:69]
	s_mov_b32 m0, s67
	s_nop 0
	s_mov_b32 s67, m0
	s_mov_b32 m0, s50
	s_nop 0
	global_load_lds_dwordx4 v87, s[40:41]
	s_mov_b32 m0, s67
	s_nop 0
	s_mov_b32 s67, m0
	s_mov_b32 m0, s55
	s_nop 0
	global_load_lds_dwordx4 v88, s[40:41]
	s_mov_b32 m0, s67
	s_waitcnt vmcnt(6)
	s_waitcnt lgkmcnt(0)
	s_barrier
	s_barrier
; #define PG8_STAGEB(bufoff, gbase) PG8_STAGE2(bufoff, gbase, voffB[0], voffB[1])
; #define PG8_STAGEAS(bufoff, gbase, h) PG8_STAGE2(bufoff, gbase, voffA[h][0], voffA[h][1])
; #define PG8_LDA(dst, b, h) do { _Pragma("unroll") for (int m = 0; m < 4; ++m) _Pragma("unroll") for (int k = 0; k < 2; ++k) dst[m][k] = *(const LAS bf16x8*)(lds + PG8_SA(b, h) + aoff + m * 2048 + k * 1024); } while (0)
; #define PG8_LDB(dst, b, h) do { _Pragma("unroll") for (int n = 0; n < 2; ++n) _Pragma("unroll") for (int k = 0; k < 2; ++k) dst[n][k] = *(const LAS bf16x8*)(lds + PG8_SB(b, h) + boff + n * 2048 + k * 1024); } while (0)
; #define PG8_WAIT_K() do { if constexpr (HM) PG8_WAIT_V(6); else PG8_WAIT_V(8); } while (0)
; #define PG8_WAIT_L(n) asm volatile("s_waitcnt lgkmcnt(" #n ")" ::: "memory")
; #define PG8_BAR __builtin_amdgcn_s_barrier()
; #define PG8_SCHED __builtin_amdgcn_sched_barrier(0)
;     ...
;             PG8_LDB(B0, 1, 0); PG8_LDB(B1, 1, 1); PG8_SCHED; PG8_LDA(At, 1, 0); if constexpr (!HM) PG8_STAGEAS(PG8_SA(0, 1), a2, 1);
;             PG8_WAIT_K(); PG8_WAIT_L(0); PG8_BAR; PG8_MMA(0, 0, At, B0); PG8_MMA(0, 1, At, B1); PG8_BAR; PG8_SCHED;
;             if constexpr (!HM) PG8_LDA(At, 1, 1);
;             PG8_STAGEB(PG8_SB(1, 0), b3); PG8_STAGEB(PG8_SB(1, 1), b3 + hstepB); PG8_STAGEAS(PG8_SA(1, 0), a3, 0);
;             PG8_WAIT_K(); PG8_WAIT_L(0); PG8_BAR; if constexpr (!HM) { PG8_MMA(1, 0, At, B0); PG8_MMA(1, 1, At, B1); } PG8_BAR; PG8_SCHED;
	ds_read_b128 v[68:71], v103
	ds_read_b128 v[72:75], v103 offset:1024
	ds_read_b128 v[76:79], v103 offset:2048
	ds_read_b128 v[80:83], v103 offset:3072
	ds_read_b128 v[106:109], v104
	ds_read_b128 v[110:113], v104 offset:1024
	ds_read_b128 v[114:117], v104 offset:2048
	ds_read_b128 v[118:121], v104 offset:3072
	ds_read_b128 v[122:125], v102 offset:32768
	ds_read_b128 v[126:129], v102 offset:33792
	ds_read_b128 v[130:133], v102 offset:34816
	ds_read_b128 v[134:137], v102 offset:35840
	ds_read_b128 v[138:141], v102 offset:36864
	ds_read_b128 v[142:145], v102 offset:37888
	ds_read_b128 v[146:149], v102 offset:38912
	ds_read_b128 v[150:153], v102 offset:39936
	s_waitcnt vmcnt(6)
	s_waitcnt lgkmcnt(0)
	s_barrier
	s_setprio 0
	s_waitcnt lgkmcnt(6)
	v_mfma_scale_f32_16x16x128_f8f6f4 v[62:65], v[68:75], v[122:129], v[62:65], v1, v86 op_sel_hi:[0,0,0]
	v_mfma_scale_f32_16x16x128_f8f6f4 v[58:61], v[76:83], v[122:129], v[58:61], v1, v86 op_sel_hi:[0,0,0]
	s_waitcnt lgkmcnt(4)
	v_mfma_scale_f32_16x16x128_f8f6f4 v[46:49], v[68:75], v[130:137], v[46:49], v1, v86 op_sel_hi:[0,0,0]
	v_mfma_scale_f32_16x16x128_f8f6f4 v[42:45], v[76:83], v[130:137], v[42:45], v1, v86 op_sel_hi:[0,0,0]
	s_waitcnt lgkmcnt(2)
	v_mfma_scale_f32_16x16x128_f8f6f4 v[30:33], v[68:75], v[138:145], v[30:33], v1, v86 op_sel_hi:[0,0,0]
	v_mfma_scale_f32_16x16x128_f8f6f4 v[26:29], v[76:83], v[138:145], v[26:29], v1, v86 op_sel_hi:[0,0,0]
	s_waitcnt lgkmcnt(0)
	v_mfma_scale_f32_16x16x128_f8f6f4 v[14:17], v[68:75], v[146:153], v[14:17], v1, v86 op_sel_hi:[0,0,0]
	v_mfma_scale_f32_16x16x128_f8f6f4 v[10:13], v[76:83], v[146:153], v[10:13], v1, v86 op_sel_hi:[0,0,0]
	s_setprio 1
	s_setprio 0
	s_add_u32 s40, s38, 0x80
	v_mfma_scale_f32_16x16x128_f8f6f4 v[54:57], v[106:113], v[122:129], v[54:57], v1, v86 op_sel_hi:[0,0,0]
	v_mfma_scale_f32_16x16x128_f8f6f4 v[50:53], v[114:121], v[122:129], v[50:53], v1, v86 op_sel_hi:[0,0,0]
	v_mfma_scale_f32_16x16x128_f8f6f4 v[38:41], v[106:113], v[130:137], v[38:41], v1, v86 op_sel_hi:[0,0,0]
	v_mfma_scale_f32_16x16x128_f8f6f4 v[34:37], v[114:121], v[130:137], v[34:37], v1, v86 op_sel_hi:[0,0,0]
	v_mfma_scale_f32_16x16x128_f8f6f4 v[22:25], v[106:113], v[138:145], v[22:25], v1, v86 op_sel_hi:[0,0,0]
	v_mfma_scale_f32_16x16x128_f8f6f4 v[18:21], v[114:121], v[138:145], v[18:21], v1, v86 op_sel_hi:[0,0,0]
	v_mfma_scale_f32_16x16x128_f8f6f4 v[6:9], v[106:113], v[146:153], v[6:9], v1, v86 op_sel_hi:[0,0,0]
	v_mfma_scale_f32_16x16x128_f8f6f4 v[2:5], v[114:121], v[146:153], v[2:5], v1, v86 op_sel_hi:[0,0,0]
	s_addc_u32 s41, s39, 0
	s_setprio 1
	s_barrier
	s_mov_b32 s67, m0
	s_mov_b32 m0, s56
	s_nop 0
	global_load_lds_dwordx4 v89, s[40:41]
	s_mov_b32 m0, s67
	s_add_u32 s38, s38, 0x40080
	s_mov_b32 s67, m0
	s_mov_b32 m0, s57
	s_nop 0
	global_load_lds_dwordx4 v90, s[40:41]
	s_mov_b32 m0, s67
	s_addc_u32 s39, s39, 0
	s_mov_b32 s40, m0
	s_mov_b32 m0, s60
	s_nop 0
	global_load_lds_dwordx4 v89, s[38:39]
	s_mov_b32 m0, s40
	s_nop 0
	s_mov_b32 s40, m0
	s_mov_b32 m0, s61
	s_nop 0
	global_load_lds_dwordx4 v90, s[38:39]
	s_mov_b32 m0, s40
	s_mov_b32 s38, m0
	s_mov_b32 m0, s58
	s_nop 0
	global_load_lds_dwordx4 v87, s[36:37]
	s_mov_b32 m0, s38
	s_nop 0
	s_mov_b32 s38, m0
	s_mov_b32 m0, s59
	s_nop 0
	global_load_lds_dwordx4 v88, s[36:37]
	s_mov_b32 m0, s38
	s_waitcnt vmcnt(6)
	s_waitcnt lgkmcnt(0)
	s_barrier
	s_barrier
	s_add_i32 s66, s66, 2
	s_add_u32 s25, s25, 0x100
	s_addc_u32 s29, s29, 0
	s_add_u32 s31, s31, 0x100
	s_addc_u32 s65, s65, 0
	s_cmp_gt_u32 s66, 13
	s_cbranch_scc0 .LBB0_1346
	s_and_b64 vcc, exec, s[20:21]
	s_cbranch_vccz .LBB0_1349
	s_barrier
